# stack9
# speedup vs baseline: 1.0025x; 1.0000x over previous
_Z6k_rec2PKiS0_S0_PK15HIP_vector_typeIjLj4EEPKfS6_PS2_PS1_IjLj2EEPf:
	v_readfirstlane_b32 s90, v0
	s_lshr_b32 s90, s90, 8
	s_load_dwordx2 s[6:7], s[0:1], 0x0
	s_load_dwordx2 s[4:5], s[0:1], 0x28
	s_load_dwordx4 s[72:75], s[0:1], 0x8
	v_cmp_gt_u32_e32 vcc, 32, v0
	s_and_saveexec_b64 s[8:9], vcc
	v_mov_b32_e32 v1, 0x22000
	v_lshl_or_b32 v1, v0, 2, v1
	v_mov_b32_e32 v2, 0
	ds_write_b32 v1, v2
	s_or_b64 exec, exec, s[8:9]
	v_mov_b32_e32 v3, 0
	v_lshlrev_b32_e32 v2, 2, v0
	s_waitcnt lgkmcnt(0)
	v_lshrrev_b32_e32 v214, 1, v0
	v_and_b32_e32 v214, 0xe0, v214
	global_load_dwordx4 v[216:219], v214, s[74:75]
	global_load_dwordx4 v[220:223], v214, s[72:73]
	global_load_dwordx3 v[224:226], v214, s[74:75] offset:16
	global_load_dwordx3 v[198:200], v214, s[72:73] offset:16
	global_load_dword v227, v214, s[74:75] offset:28
	global_load_dword v228, v214, s[72:73] offset:28
	v_lshl_add_u64 v[4:5], s[6:7], 0, v[2:3]
	s_movk_i32 s3, 0x1000
	v_or_b32_e32 v1, 0x400, v0
	v_add_co_u32_e32 v6, vcc, s3, v4
	v_lshlrev_b32_e32 v3, 2, v1
	s_nop 0
	v_addc_co_u32_e32 v7, vcc, 0, v5, vcc
	global_load_dword v68, v2, s[6:7]
	global_load_dword v69, v2, s[6:7] offset:2048
	global_load_dword v70, v3, s[6:7]
	global_load_dword v71, v[6:7], off offset:2048
	v_or_b32_e32 v165, 0x800, v0
	s_movk_i32 s3, 0x2000
	v_lshlrev_b32_e32 v6, 2, v165
	v_add_co_u32_e32 v2, vcc, s3, v4
	v_or_b32_e32 v232, 0xc00, v0
	s_nop 0
	v_addc_co_u32_e32 v3, vcc, 0, v5, vcc
	global_load_dword v72, v6, s[6:7]
	global_load_dword v73, v[2:3], off offset:2048
	v_lshlrev_b32_e32 v2, 2, v232
	global_load_dword v74, v2, s[6:7]
	s_movk_i32 s3, 0x3000
	v_add_co_u32_e32 v2, vcc, s3, v4
	s_ashr_i32 s3, s2, 31
	s_nop 0
	v_addc_co_u32_e32 v3, vcc, 0, v5, vcc
	global_load_dword v75, v[2:3], off offset:2048
	s_lshl_b64 s[6:7], s[2:3], 17
	s_add_u32 s4, s4, s6
	s_addc_u32 s5, s5, s7
	v_mbcnt_lo_u32_b32 v77, -1, 0
	v_mbcnt_hi_u32_b32 v77, -1, v77
	v_and_b32_e32 v83, 64, v77
	v_xor_b32_e32 v84, 32, v77
	v_add_u32_e32 v83, 64, v83
	v_cmp_lt_i32_e32 vcc, v84, v83
	v_xor_b32_e32 v85, 16, v77
	v_xor_b32_e32 v86, 8, v77
	v_cndmask_b32_e32 v84, v77, v84, vcc
	v_lshlrev_b32_e32 v234, 2, v84
	v_cmp_lt_i32_e32 vcc, v85, v83
	v_xor_b32_e32 v87, 4, v77
	v_xor_b32_e32 v88, 2, v77
	v_cndmask_b32_e32 v85, v77, v85, vcc
	v_lshlrev_b32_e32 v235, 2, v85
	v_cmp_lt_i32_e32 vcc, v86, v83
	v_xor_b32_e32 v89, 1, v77
	v_mov_b32_e32 v76, 0x20000
	v_cndmask_b32_e32 v86, v77, v86, vcc
	v_lshlrev_b32_e32 v236, 2, v86
	v_cmp_lt_i32_e32 vcc, v87, v83
	v_lshl_or_b32 v79, v1, 1, v76
	v_lshl_or_b32 v81, v165, 1, v76
	v_cndmask_b32_e32 v87, v77, v87, vcc
	v_cmp_lt_i32_e32 vcc, v88, v83
	v_lshlrev_b32_e32 v237, 2, v87
	v_lshl_or_b32 v76, v232, 1, v76
	v_cndmask_b32_e32 v88, v77, v88, vcc
	v_cmp_lt_i32_e32 vcc, v89, v83
	v_lshlrev_b32_e32 v238, 2, v88
	s_mov_b32 s3, 0
	v_cndmask_b32_e32 v77, v77, v89, vcc
	v_lshlrev_b32_e32 v239, 2, v77
	s_waitcnt vmcnt(7)
	v_lshlrev_b32_e32 v2, 1, v68
	s_waitcnt vmcnt(6)
	v_lshlrev_b32_e32 v4, 1, v69
	v_ashrrev_i32_e32 v3, 31, v2
	v_ashrrev_i32_e32 v5, 31, v4
	v_lshl_add_u64 v[10:11], v[2:3], 4, s[4:5]
	v_lshl_add_u64 v[20:21], v[4:5], 4, s[4:5]
	global_load_dwordx4 v[2:5], v[10:11], off offset:16
	global_load_dwordx4 v[6:9], v[10:11], off
	s_nop 0
	global_load_dwordx4 v[10:13], v[20:21], off offset:16
	global_load_dwordx4 v[14:17], v[20:21], off
	s_waitcnt vmcnt(9)
	v_lshlrev_b32_e32 v18, 1, v70
	v_ashrrev_i32_e32 v19, 31, v18
	v_lshl_add_u64 v[28:29], v[18:19], 4, s[4:5]
	global_load_dwordx4 v[18:21], v[28:29], off offset:16
	global_load_dwordx4 v[22:25], v[28:29], off
	s_waitcnt vmcnt(10)
	v_lshlrev_b32_e32 v26, 1, v71
	v_ashrrev_i32_e32 v27, 31, v26
	v_lshl_add_u64 v[36:37], v[26:27], 4, s[4:5]
	global_load_dwordx4 v[26:29], v[36:37], off offset:16
	global_load_dwordx4 v[30:33], v[36:37], off
	s_waitcnt vmcnt(11)
	v_lshlrev_b32_e32 v34, 1, v72
	v_ashrrev_i32_e32 v35, 31, v34
	v_lshl_add_u64 v[44:45], v[34:35], 4, s[4:5]
	global_load_dwordx4 v[34:37], v[44:45], off offset:16
	global_load_dwordx4 v[38:41], v[44:45], off
	s_waitcnt vmcnt(12)
	v_lshlrev_b32_e32 v42, 1, v73
	v_ashrrev_i32_e32 v43, 31, v42
	v_lshl_add_u64 v[52:53], v[42:43], 4, s[4:5]
	global_load_dwordx4 v[42:45], v[52:53], off offset:16
	global_load_dwordx4 v[46:49], v[52:53], off
	s_waitcnt vmcnt(13)
	v_lshlrev_b32_e32 v50, 1, v74
	v_ashrrev_i32_e32 v51, 31, v50
	v_lshl_add_u64 v[58:59], v[50:51], 4, s[4:5]
	global_load_dwordx4 v[50:53], v[58:59], off offset:16
	global_load_dwordx4 v[54:57], v[58:59], off
	s_waitcnt vmcnt(14)
	v_lshlrev_b32_e32 v58, 1, v75
	v_ashrrev_i32_e32 v59, 31, v58
	v_lshl_add_u64 v[66:67], v[58:59], 4, s[4:5]
	global_load_dwordx4 v[62:65], v[66:67], off
	global_load_dwordx4 v[58:61], v[66:67], off offset:16
	v_lshlrev_b32_e32 v67, 1, v0
	v_or_b32_e32 v233, 0x20000, v67
	s_load_dwordx4 s[8:11], s[0:1], 0x8
	s_load_dwordx2 s[14:15], s[0:1], 0x18
	s_load_dwordx2 s[12:13], s[0:1], 0x40
	s_load_dwordx2 s[6:7], s[0:1], 0x30
	v_or_b32_e32 v78, 0x20400, v67
	v_or_b32_e32 v80, 0x20c00, v67
	ds_write_b16 v233, v68
	ds_write_b16 v78, v69
	ds_write_b16 v79, v70
	ds_write_b16 v80, v71
	v_or_b32_e32 v82, 0x21400, v67
	v_or_b32_e32 v67, 0x21c00, v67
	ds_write_b16 v81, v72
	ds_write_b16 v82, v73
	ds_write_b16 v76, v74
	ds_write_b16 v67, v75
	v_and_b32_e32 v66, 63, v0
	v_cmp_eq_u32_e64 s[4:5], 0, v66
	s_waitcnt lgkmcnt(0)
	s_barrier
	s_waitcnt vmcnt(14)
	v_max3_f32 v84, |v6|, 0, |v7|
	v_max3_f32 v84, v84, |v8|, |v9|
	v_max3_f32 v84, v84, |v2|, |v3|
	v_max3_f32 v84, v84, |v4|, |v5|
	s_waitcnt vmcnt(12)
	v_max3_f32 v84, v84, |v14|, |v15|
	v_max3_f32 v84, v84, |v16|, |v17|
	v_max3_f32 v84, v84, |v10|, |v11|
	v_max3_f32 v84, v84, |v12|, |v13|
	s_waitcnt vmcnt(10)
	v_max3_f32 v84, v84, |v22|, |v23|
	v_max3_f32 v84, v84, |v24|, |v25|
	v_max3_f32 v84, v84, |v18|, |v19|
	v_max3_f32 v84, v84, |v20|, |v21|
	s_waitcnt vmcnt(8)
	v_max3_f32 v84, v84, |v30|, |v31|
	v_max3_f32 v84, v84, |v32|, |v33|
	v_max3_f32 v84, v84, |v26|, |v27|
	v_max3_f32 v84, v84, |v28|, |v29|
	s_waitcnt vmcnt(6)
	v_max3_f32 v84, v84, |v38|, |v39|
	v_max3_f32 v84, v84, |v40|, |v41|
	v_max3_f32 v84, v84, |v34|, |v35|
	v_max3_f32 v84, v84, |v36|, |v37|
	s_waitcnt vmcnt(4)
	v_max3_f32 v84, v84, |v46|, |v47|
	v_max3_f32 v84, v84, |v48|, |v49|
	v_max3_f32 v84, v84, |v42|, |v43|
	v_max3_f32 v84, v84, |v44|, |v45|
	s_waitcnt vmcnt(2)
	v_max3_f32 v84, v84, |v54|, |v55|
	v_max3_f32 v84, v84, |v56|, |v57|
	v_max3_f32 v84, v84, |v50|, |v51|
	v_max3_f32 v84, v84, |v52|, |v53|
	s_waitcnt vmcnt(1)
	v_max3_f32 v84, v84, |v62|, |v63|
	v_max3_f32 v84, v84, |v64|, |v65|
	s_waitcnt vmcnt(0)
	v_max3_f32 v84, v84, |v58|, |v59|
	v_max3_f32 v84, v84, |v60|, |v61|
	ds_bpermute_b32 v90, v234, v84
	s_waitcnt lgkmcnt(0)
	v_max_f32_e32 v85, v90, v90
	v_max_f32_e32 v84, v84, v85
	ds_bpermute_b32 v85, v235, v84
	s_waitcnt lgkmcnt(0)
	v_max_f32_e32 v85, v85, v85
	v_max_f32_e32 v84, v84, v85
	ds_bpermute_b32 v85, v236, v84
	s_waitcnt lgkmcnt(0)
	v_max_f32_e32 v83, v85, v85
	v_max_f32_e32 v83, v84, v83
	ds_bpermute_b32 v84, v237, v83
	s_waitcnt lgkmcnt(0)
	v_max_f32_e32 v68, v84, v84
	v_max_f32_e32 v68, v83, v68
	ds_bpermute_b32 v69, v238, v68
	s_waitcnt lgkmcnt(0)
	v_max_f32_e32 v67, v69, v69
	v_max_f32_e32 v67, v68, v67
	ds_bpermute_b32 v68, v239, v67
	s_and_saveexec_b64 s[16:17], s[4:5]
	s_cbranch_execz .LBB3_7
	s_waitcnt lgkmcnt(0)
	v_max_f32_e32 v68, v68, v68
	v_max_f32_e32 v67, v67, v67
	s_mov_b64 s[18:19], exec
	v_max_f32_e32 v67, v67, v68

.LBB3_7:
	s_or_b64 exec, exec, s[16:17]
	v_mov_b32_e32 v67, 0x22000
	s_waitcnt lgkmcnt(0)
	s_barrier
	ds_read_b32 v67, v67
	ds_read_u16 v72, v233
	s_load_dwordx2 s[18:19], s[0:1], 0x38
	s_mov_b32 s0, 0xc77fe000
	v_mov_b32_e32 v73, 0x477fe000
	s_waitcnt lgkmcnt(0)
	v_bfe_u32 v67, v67, 23, 8
	v_max_u32_e32 v67, 11, v67
	v_lshlrev_b32_e32 v79, 23, v67
	v_sub_u32_e32 v164, 0x84000000, v79
	v_mul_f32_e32 v70, v9, v164
	v_mul_f32_e32 v71, v3, v164
	v_mul_f32_e32 v67, v6, v164
	v_mul_f32_e32 v68, v7, v164
	v_mul_f32_e32 v69, v8, v164
	v_med3_f32 v74, v70, s0, v73
	v_mul_f32_e32 v70, v2, v164
	v_med3_f32 v75, v71, s0, v73
	v_mul_f32_e32 v71, v4, v164
	v_mul_f32_e32 v76, v5, v164
	v_med3_f32 v67, v67, s0, v73
	v_med3_f32 v68, v68, s0, v73
	v_med3_f32 v69, v69, s0, v73
	v_med3_f32 v70, v70, s0, v73
	v_med3_f32 v71, v71, s0, v73
	v_med3_f32 v76, v76, s0, v73
	v_cvt_pk_f16_f32 v71, v71, v76
	v_cvt_pk_f16_f32 v70, v70, v75
	v_cvt_pk_f16_f32 v69, v69, v74
	v_cvt_pk_f16_f32 v68, v67, v68
	v_lshlrev_b32_e32 v67, 4, v72
	ds_write_b128 v67, v[68:71]
	ds_read_u16 v67, v233 offset:1024
	v_mul_f32_e32 v69, v15, v164
	v_mul_f32_e32 v70, v17, v164
	v_mul_f32_e32 v71, v11, v164
	v_mul_f32_e32 v68, v14, v164
	v_med3_f32 v72, v69, s0, v73
	v_mul_f32_e32 v69, v16, v164
	v_med3_f32 v74, v70, s0, v73
	v_mul_f32_e32 v70, v10, v164
	v_med3_f32 v75, v71, s0, v73
	v_mul_f32_e32 v71, v12, v164
	v_mul_f32_e32 v76, v13, v164
	v_med3_f32 v68, v68, s0, v73
	v_med3_f32 v69, v69, s0, v73
	v_med3_f32 v70, v70, s0, v73
	v_med3_f32 v71, v71, s0, v73
	v_med3_f32 v76, v76, s0, v73
	v_cvt_pk_f16_f32 v71, v71, v76
	v_cvt_pk_f16_f32 v70, v70, v75
	v_cvt_pk_f16_f32 v69, v69, v74
	v_cvt_pk_f16_f32 v68, v68, v72
	s_waitcnt lgkmcnt(0)
	v_lshlrev_b32_e32 v67, 4, v67
	ds_write_b128 v67, v[68:71]
	ds_read_u16 v67, v233 offset:2048
	v_mul_f32_e32 v69, v23, v164
	v_mul_f32_e32 v70, v25, v164
	v_mul_f32_e32 v71, v19, v164
	v_mul_f32_e32 v68, v22, v164
	v_med3_f32 v72, v69, s0, v73
	v_mul_f32_e32 v69, v24, v164
	v_med3_f32 v74, v70, s0, v73
	v_mul_f32_e32 v70, v18, v164
	v_med3_f32 v75, v71, s0, v73
	v_mul_f32_e32 v71, v20, v164
	v_mul_f32_e32 v76, v21, v164
	v_med3_f32 v68, v68, s0, v73
	v_med3_f32 v69, v69, s0, v73
	v_med3_f32 v70, v70, s0, v73
	v_med3_f32 v71, v71, s0, v73
	v_med3_f32 v76, v76, s0, v73
	v_cvt_pk_f16_f32 v71, v71, v76
	v_cvt_pk_f16_f32 v70, v70, v75
	v_cvt_pk_f16_f32 v69, v69, v74
	v_cvt_pk_f16_f32 v68, v68, v72
	s_waitcnt lgkmcnt(0)
	v_lshlrev_b32_e32 v67, 4, v67
	ds_write_b128 v67, v[68:71]
	ds_read_u16 v67, v233 offset:3072
	v_mul_f32_e32 v69, v31, v164
	v_mul_f32_e32 v70, v33, v164
	v_mul_f32_e32 v71, v27, v164
	v_mul_f32_e32 v68, v30, v164
	v_med3_f32 v72, v69, s0, v73
	v_mul_f32_e32 v69, v32, v164
	v_med3_f32 v74, v70, s0, v73
	v_mul_f32_e32 v70, v26, v164
	v_med3_f32 v75, v71, s0, v73
	v_mul_f32_e32 v71, v28, v164
	v_mul_f32_e32 v76, v29, v164
	v_med3_f32 v68, v68, s0, v73
	v_med3_f32 v69, v69, s0, v73
	v_med3_f32 v70, v70, s0, v73
	v_med3_f32 v71, v71, s0, v73
	v_med3_f32 v76, v76, s0, v73
	v_cvt_pk_f16_f32 v71, v71, v76
	v_cvt_pk_f16_f32 v70, v70, v75
	v_cvt_pk_f16_f32 v69, v69, v74
	v_cvt_pk_f16_f32 v68, v68, v72
	s_waitcnt lgkmcnt(0)
	v_lshlrev_b32_e32 v67, 4, v67
	ds_write_b128 v67, v[68:71]
	ds_read_u16 v67, v233 offset:4096
	v_mul_f32_e32 v69, v39, v164
	v_mul_f32_e32 v70, v41, v164
	v_mul_f32_e32 v71, v35, v164
	v_mul_f32_e32 v68, v38, v164
	v_med3_f32 v72, v69, s0, v73
	v_mul_f32_e32 v69, v40, v164
	v_med3_f32 v74, v70, s0, v73
	v_mul_f32_e32 v70, v34, v164
	v_med3_f32 v75, v71, s0, v73
	v_mul_f32_e32 v71, v36, v164
	v_mul_f32_e32 v76, v37, v164
	v_med3_f32 v68, v68, s0, v73
	v_med3_f32 v69, v69, s0, v73
	v_med3_f32 v70, v70, s0, v73
	v_med3_f32 v71, v71, s0, v73
	v_med3_f32 v76, v76, s0, v73
	v_cvt_pk_f16_f32 v71, v71, v76
	v_cvt_pk_f16_f32 v70, v70, v75
	v_cvt_pk_f16_f32 v69, v69, v74
	v_cvt_pk_f16_f32 v68, v68, v72
	s_waitcnt lgkmcnt(0)
	v_lshlrev_b32_e32 v67, 4, v67
	ds_write_b128 v67, v[68:71]
	ds_read_u16 v67, v233 offset:5120
	v_mul_f32_e32 v69, v47, v164
	v_mul_f32_e32 v70, v49, v164
	v_mul_f32_e32 v71, v43, v164
	v_mul_f32_e32 v68, v46, v164
	v_med3_f32 v72, v69, s0, v73
	v_mul_f32_e32 v69, v48, v164
	v_med3_f32 v74, v70, s0, v73
	v_mul_f32_e32 v70, v42, v164
	v_med3_f32 v75, v71, s0, v73
	v_mul_f32_e32 v71, v44, v164
	v_mul_f32_e32 v76, v45, v164
	v_med3_f32 v68, v68, s0, v73
	v_med3_f32 v69, v69, s0, v73
	v_med3_f32 v70, v70, s0, v73
	v_med3_f32 v71, v71, s0, v73
	v_med3_f32 v76, v76, s0, v73
	v_cvt_pk_f16_f32 v71, v71, v76
	v_cvt_pk_f16_f32 v70, v70, v75
	v_cvt_pk_f16_f32 v69, v69, v74
	v_cvt_pk_f16_f32 v68, v68, v72
	s_waitcnt lgkmcnt(0)
	v_lshlrev_b32_e32 v67, 4, v67
	ds_write_b128 v67, v[68:71]
	ds_read_u16 v67, v233 offset:6144
	v_mul_f32_e32 v69, v55, v164
	v_mul_f32_e32 v70, v57, v164
	v_mul_f32_e32 v71, v51, v164
	v_mul_f32_e32 v68, v54, v164
	v_med3_f32 v72, v69, s0, v73
	v_mul_f32_e32 v69, v56, v164
	v_med3_f32 v74, v70, s0, v73
	v_mul_f32_e32 v70, v50, v164
	v_med3_f32 v75, v71, s0, v73
	v_mul_f32_e32 v71, v52, v164
	v_mul_f32_e32 v76, v53, v164
	v_med3_f32 v68, v68, s0, v73
	v_med3_f32 v69, v69, s0, v73
	v_med3_f32 v70, v70, s0, v73
	v_med3_f32 v71, v71, s0, v73
	v_med3_f32 v76, v76, s0, v73
	v_cvt_pk_f16_f32 v71, v71, v76
	v_cvt_pk_f16_f32 v70, v70, v75
	v_cvt_pk_f16_f32 v69, v69, v74
	v_cvt_pk_f16_f32 v68, v68, v72
	s_waitcnt lgkmcnt(0)
	v_lshlrev_b32_e32 v67, 4, v67
	ds_write_b128 v67, v[68:71]
	ds_read_u16 v67, v233 offset:7168
	v_mul_f32_e32 v69, v63, v164
	v_mul_f32_e32 v70, v65, v164
	v_mul_f32_e32 v71, v59, v164
	v_mul_f32_e32 v68, v62, v164
	v_med3_f32 v72, v69, s0, v73
	v_mul_f32_e32 v69, v64, v164
	v_med3_f32 v74, v70, s0, v73
	v_mul_f32_e32 v70, v58, v164
	v_med3_f32 v75, v71, s0, v73
	v_mul_f32_e32 v71, v60, v164
	v_mul_f32_e32 v76, v61, v164
	v_med3_f32 v68, v68, s0, v73
	v_med3_f32 v69, v69, s0, v73
	v_med3_f32 v70, v70, s0, v73
	v_med3_f32 v71, v71, s0, v73
	v_med3_f32 v73, v76, s0, v73
	v_cvt_pk_f16_f32 v71, v71, v73
	v_cvt_pk_f16_f32 v70, v70, v75
	v_cvt_pk_f16_f32 v69, v69, v74
	v_cvt_pk_f16_f32 v68, v68, v72
	s_waitcnt lgkmcnt(0)
	v_lshlrev_b32_e32 v67, 4, v67
	ds_write_b128 v67, v[68:71]
	v_lshrrev_b32_e32 v67, 1, v0
	v_and_b32_e32 v83, 0xe0, v67
	s_waitcnt lgkmcnt(0)
	s_barrier
	s_movk_i32 s0, 0xfc
	v_bitop3_b32 v67, v67, s0, 28 bitop3:0xc8
	s_ashr_i32 s43, s2, 2
	s_and_b32 s33, s2, 3
	s_mul_i32 s8, s43, 0x4c
	v_mov_b32_e32 v103, 0
	v_lshlrev_b32_e32 v104, 4, v66
	v_mov_b32_e32 v105, v103
	v_lshl_add_u64 v[66:67], s[14:15], 0, v[104:105]
	v_lshlrev_b32_e32 v102, 3, v0
	v_mov_b32_e32 v132, v103
	v_mov_b32_e32 v133, v103
	s_mov_b32 s34, 1
	v_mov_b32_e32 v105, 0xfff0
	v_add_u32_e32 v230, 0xfb000000, v79
	s_mov_b32 s9, 0
	v_cmp_eq_u32_e64 s[2:3], 0, v0
	s_mov_b32 s63, 0x43800000
	s_movk_i32 s64, 0x2000
	s_movk_i32 s65, 0x6000
	s_mov_b32 s66, 0xa000
	v_mov_b64_e32 v[134:135], v[132:133]
	v_mov_b64_e32 v[136:137], v[132:133]
	v_mov_b64_e32 v[138:139], v[132:133]
	v_mov_b64_e32 v[140:141], v[132:133]
	v_mov_b64_e32 v[142:143], v[132:133]
	v_mov_b64_e32 v[144:145], v[132:133]
	v_mov_b64_e32 v[146:147], v[132:133]
	v_mov_b64_e32 v[156:157], v[132:133]
	v_mov_b64_e32 v[158:159], v[132:133]
	v_mov_b64_e32 v[160:161], v[132:133]
	v_mov_b64_e32 v[162:163], v[132:133]
	v_mov_b64_e32 v[166:167], v[132:133]
	v_mov_b64_e32 v[168:169], v[132:133]
	v_mov_b64_e32 v[170:171], v[132:133]
	v_mov_b64_e32 v[172:173], v[132:133]
	v_mov_b64_e32 v[174:175], v[132:133]
	v_mov_b64_e32 v[176:177], v[132:133]
	v_mov_b64_e32 v[178:179], v[132:133]
	v_mov_b64_e32 v[180:181], v[132:133]
	v_mov_b64_e32 v[190:191], v[132:133]
	v_mov_b64_e32 v[192:193], v[132:133]
	v_mov_b64_e32 v[194:195], v[132:133]
	v_mov_b64_e32 v[196:197], v[132:133]
	v_mov_b64_e32 v[206:207], v[132:133]
	v_mov_b64_e32 v[208:209], v[132:133]
	v_mov_b64_e32 v[210:211], v[132:133]
	v_mov_b64_e32 v[212:213], v[132:133]
	v_mov_b64_e32 v[148:149], v[132:133]
	v_mov_b64_e32 v[150:151], v[132:133]
	v_mov_b64_e32 v[152:153], v[132:133]
	v_mov_b64_e32 v[154:155], v[132:133]
	s_waitcnt vmcnt(5)
	v_readfirstlane_b32 s0, v216
	s_ashr_i32 s10, s0, 2
	s_waitcnt vmcnt(4)
	v_readfirstlane_b32 s0, v220
	v_readfirstlane_b32 s1, v217
	s_ashr_i32 s16, s1, 2
	v_readfirstlane_b32 s1, v221
	s_ashr_i32 s36, s0, 2
	v_readfirstlane_b32 s0, v218
	s_ashr_i32 s35, s1, 2
	s_ashr_i32 s20, s0, 2
	v_readfirstlane_b32 s0, v222
	v_readfirstlane_b32 s1, v219
	s_ashr_i32 s22, s1, 2
	v_readfirstlane_b32 s1, v223
	s_ashr_i32 s37, s0, 2
	s_waitcnt vmcnt(3)
	v_readfirstlane_b32 s0, v224
	s_ashr_i32 s38, s1, 2
	s_ashr_i32 s24, s0, 2
	s_waitcnt vmcnt(2)
	v_readfirstlane_b32 s0, v198
	v_readfirstlane_b32 s1, v225
	s_ashr_i32 s26, s1, 2
	v_readfirstlane_b32 s1, v199
	s_ashr_i32 s40, s0, 2
	v_readfirstlane_b32 s0, v226
	s_ashr_i32 s39, s1, 2
	s_ashr_i32 s28, s0, 2
	v_readfirstlane_b32 s0, v200
	s_waitcnt vmcnt(1)
	v_readfirstlane_b32 s1, v227
	s_ashr_i32 s30, s1, 2
	s_waitcnt vmcnt(0)
	v_readfirstlane_b32 s1, v228
	s_ashr_i32 s41, s0, 2
	s_mul_i32 s0, s43, 0x64
	s_ashr_i32 s42, s1, 2
	s_ashr_i32 s1, s0, 31
	s_lshl_b64 s[0:1], s[0:1], 2
	s_add_u32 s0, s12, s0
	s_addc_u32 s1, s13, s1
	s_mul_i32 s43, s43, 24
	s_ashr_i32 s11, s10, 31
	s_ashr_i32 s17, s16, 31
	s_ashr_i32 s21, s20, 31
	s_ashr_i32 s23, s22, 31
	s_add_i32 s44, s43, 0xffffffb4
	s_lshl_b64 s[12:13], s[10:11], 4
	s_lshl_b64 s[16:17], s[16:17], 4
	s_lshl_b64 s[20:21], s[20:21], 4
	s_lshl_b64 s[22:23], s[22:23], 4
	s_cmp_lt_i32 s36, 1
	s_cselect_b64 s[10:11], -1, 0
	s_add_u32 s45, s14, s12
	s_addc_u32 s46, s15, s13
	s_add_u32 s47, s14, s16
	s_addc_u32 s48, s15, s17
	s_add_u32 s49, s14, s20
	s_addc_u32 s50, s15, s21
	s_add_u32 s51, s14, s22
	s_addc_u32 s52, s15, s23
	s_ashr_i32 s25, s24, 31
	s_ashr_i32 s27, s26, 31
	s_ashr_i32 s29, s28, 31
	s_ashr_i32 s31, s30, 31
	v_lshl_add_u64 v[108:109], v[66:67], 0, s[16:17]
	v_lshl_add_u64 v[110:111], v[66:67], 0, s[20:21]
	v_lshl_add_u64 v[112:113], v[66:67], 0, s[22:23]
	s_lshl_b64 s[16:17], s[24:25], 4
	s_lshl_b64 s[20:21], s[26:27], 4
	s_lshl_b64 s[22:23], s[28:29], 4
	s_lshl_b64 s[24:25], s[30:31], 4
	s_cmp_lt_i32 s40, 1
	v_lshl_add_u64 v[106:107], v[66:67], 0, s[12:13]
	s_cselect_b64 s[12:13], -1, 0
	s_add_u32 s53, s14, s16
	s_addc_u32 s54, s15, s17
	s_add_u32 s55, s14, s20
	s_addc_u32 s56, s15, s21
	s_add_u32 s57, s14, s22
	s_addc_u32 s58, s15, s23
	s_add_u32 s59, s14, s24
	s_addc_u32 s60, s15, s25
	s_cmp_lt_i32 s40, s39
	s_cselect_b64 s[14:15], -1, 0
	s_cmp_lt_i32 s36, s35
	v_lshl_add_u64 v[114:115], v[66:67], 0, s[16:17]
	v_lshl_add_u64 v[116:117], v[66:67], 0, s[20:21]
	v_lshl_add_u64 v[118:119], v[66:67], 0, s[22:23]
	v_lshl_add_u64 v[120:121], v[66:67], 0, s[24:25]
	s_cselect_b64 s[16:17], -1, 0
	v_lshl_add_u64 v[66:67], s[18:19], 0, v[102:103]
	s_mov_b64 s[18:19], 0x1000
	s_lshl_b32 s61, s36, 6
	s_lshl_b32 s62, s40, 6
	v_lshl_add_u64 v[122:123], v[66:67], 0, s[18:19]
	s_or_b32 s18, s8, s33
	v_lshlrev_b32_e32 v102, 4, v0
	s_add_i32 s61, s61, 64
	s_add_i32 s62, s62, 64
	s_mov_b64 s[20:21], 0
	s_mov_b64 s[22:23], 0x2000
